# v21 plus MoE units dealt leading full row tiles first, remainder tiles last
# baseline (speedup 1.0000x reference)
; __device__ __forceinline__ int obid() { int t = blockIdx.x; asm volatile("" : "+s"(t)); return t; }
; __device__ __forceinline__ void moe_prefix(LAS unsigned char* lds, const unsigned* cnt) {
;     ...
;     if (tz_ < 64) { const int e = tz_; const int c = (int)cnt[e], nt = (c + 255) >> 8;
;         int incl = nt;
; #pragma unroll
;         for (int o = 1; o < 64; o <<= 1) { const int up = __shfl_up(incl, o); if (e >= o) incl += up; }
;         const int excl = incl - nt;
;         s_ts[e] = excl; s_cn[e] = c;
;         for (int i = 0; i < nt; ++i) s_te[excl + i] = (unsigned char)e;
;         const int x = obid() & 7; int a2 = 0;
; #pragma unroll
;         for (int k = 0; k < 8; ++k) { const int tk = __shfl(nt, x + 8 * k); if (e == 0) s_xs[k] = a2; a2 += tk; }
;         if (e == 0) s_xs[8] = a2; }
.LBB0_877:
	s_or_b64 exec, exec, s[6:7]
	s_mov_b32 s0, s79
	v_cmp_eq_u32_e32 vcc, 0, v6
	v_and_or_b32 v2, s0, 7, v7
	v_lshlrev_b32_e32 v2, 2, v2
	v_min_u32_e32 v3, 2, v1
	v_sub_u32_e32 v4, v1, v3
	ds_bpermute_b32 v8, v2, v3
	ds_bpermute_b32 v9, v2, v3 offset:32
	ds_bpermute_b32 v10, v2, v3 offset:64
	ds_bpermute_b32 v11, v2, v3 offset:96
	ds_bpermute_b32 v12, v2, v3 offset:128
	ds_bpermute_b32 v13, v2, v3 offset:160
	ds_bpermute_b32 v14, v2, v3 offset:192
	ds_bpermute_b32 v15, v2, v3 offset:224
	ds_bpermute_b32 v16, v2, v4
	ds_bpermute_b32 v17, v2, v4 offset:32
	ds_bpermute_b32 v18, v2, v4 offset:64
	ds_bpermute_b32 v19, v2, v4 offset:96
	ds_bpermute_b32 v20, v2, v4 offset:128
	ds_bpermute_b32 v21, v2, v4 offset:160
	ds_bpermute_b32 v22, v2, v4 offset:192
	ds_bpermute_b32 v23, v2, v4 offset:224
	s_waitcnt lgkmcnt(0)
	v_add_u32_e32 v9, v9, v8
	v_add_u32_e32 v10, v10, v9
	v_add_u32_e32 v11, v11, v10
	v_add_u32_e32 v12, v12, v11
	v_add_u32_e32 v13, v13, v12
	v_add_u32_e32 v14, v14, v13
	v_add_u32_e32 v15, v15, v14
	v_add_u32_e32 v16, v16, v15
	v_add_u32_e32 v17, v17, v16
	v_add_u32_e32 v18, v18, v17
	v_add_u32_e32 v19, v19, v18
	v_add_u32_e32 v20, v20, v19
	v_add_u32_e32 v21, v21, v20
	v_add_u32_e32 v22, v22, v21
	v_add_u32_e32 v23, v23, v22
	v_mov_b32_e32 v5, 0
	s_and_b64 exec, exec, vcc
	s_cbranch_execz .LBB0_893
	v_mov_b32_e32 v3, 0x26f10
	ds_write2_b32 v3, v5, v8 offset1:1
	ds_write2_b32 v3, v9, v10 offset0:2 offset1:3
	ds_write2_b32 v3, v11, v12 offset0:4 offset1:5
	ds_write2_b32 v3, v13, v14 offset0:6 offset1:7
	ds_write2_b32 v3, v15, v16 offset0:8 offset1:9
	ds_write2_b32 v3, v17, v18 offset0:10 offset1:11
	ds_write2_b32 v3, v19, v20 offset0:12 offset1:13
	ds_write2_b32 v3, v21, v22 offset0:14 offset1:15
	ds_write_b32 v3, v23 offset:64

; #define LAS __attribute__((address_space(3)))
;     __device__ __forceinline__ bool next(int i, SkUnit& u) const { const int L = i * G + c; if (L >= (T / 256) * 4) return false; u.pm = L >> 2; u.ks = L & 3; return true; }
;     __device__ __forceinline__ bool next(int i, MUnit& u) const {
;         const LAS int* xs = (const LAS int*)((const LAS unsigned char*)ts + (LDS_XS - LDS_TS));
;         const int x = c & 7, W = G >> 3, q = i * W + (c >> 3); if ((G & 7) != 0 || q >= xs[8] * NPN) return false;
;         int k = 0; while (xs[k + 1] * NPN <= q) ++k;
;         const int e = x + 8 * k, rq = q - xs[k] * NPN, nte = xs[k + 1] - xs[k]; u.pn = rq / nte; u.mt = rq - u.pn * nte;
;         u.e = e; u.mtg = ts[e] + u.mt; u.ce = cn[e]; return true; }
.LBB0_895:
	s_add_i32 s2, 0, 0x26f50
	v_mov_b32_e32 v1, s2
	ds_read_b32 v1, v1
	s_waitcnt lgkmcnt(0)
	v_lshlrev_b32_e32 v1, 2, v1
	v_cmp_ge_i32_e32 vcc, s1, v1
	s_cbranch_vccnz .LBB0_899
	s_add_i32 s3, 0, 0x26f14
	s_mov_b32 s2, -1
.LBB0_897:
	v_mov_b32_e32 v1, s3
	ds_read_b32 v1, v1
	s_add_i32 s2, s2, 1
	s_add_i32 s3, s3, 4
	s_waitcnt lgkmcnt(0)
	v_lshlrev_b32_e32 v2, 2, v1
	v_cmp_ge_i32_e32 vcc, s1, v2
	v_readfirstlane_b32 s6, v1
	s_cbranch_vccnz .LBB0_897
	s_lshl_b32 s3, s2, 2
	s_add_i32 s3, s3, 0
	s_add_i32 s3, s3, 0x26f10
	v_mov_b32_e32 v1, s3
	ds_read_b32 v1, v1
	s_lshr_b32 s99, s2, 3
	s_and_b32 s2, s2, 7
	s_lshl_b32 s2, s2, 3
	s_or_b32 s40, s2, s0
	s_waitcnt lgkmcnt(0)
	v_readfirstlane_b32 s3, v1
	s_sub_i32 s6, s6, s3
	s_abs_i32 s7, s6
	v_cvt_f32_u32_e32 v1, s7
	s_sub_i32 s10, 0, s7
	s_lshl_b32 s2, s3, 2
	s_sub_i32 s2, s1, s2
	v_rcp_iflag_f32_e32 v1, v1
	s_abs_i32 s9, s2
	s_xor_b32 s3, s2, s6
	s_ashr_i32 s3, s3, 31
	v_mul_f32_e32 v1, 0x4f7ffffe, v1
	v_cvt_u32_f32_e32 v1, v1
	s_nop 0
	v_readfirstlane_b32 s11, v1
	s_mul_i32 s10, s10, s11
	s_mul_hi_u32 s10, s11, s10
	s_add_i32 s11, s11, s10
	s_mul_hi_u32 s10, s9, s11
	s_mul_i32 s11, s10, s7
	s_sub_i32 s9, s9, s11
	s_add_i32 s14, s10, 1
	s_sub_i32 s11, s9, s7
	s_cmp_ge_u32 s9, s7
	s_cselect_b32 s10, s14, s10
	s_cselect_b32 s9, s11, s9
	s_add_i32 s11, s10, 1
	s_cmp_ge_u32 s9, s7
	s_cselect_b32 s7, s11, s10
	s_lshl_b32 s9, s40, 2
	s_xor_b32 s7, s7, s3
	s_add_i32 s9, s9, 0
	s_sub_i32 s63, s7, s3
	s_add_i32 s3, s9, 0x26c40
	v_mov_b32_e32 v1, s3
	s_add_i32 s3, s9, 0x26d50
	ds_read_b32 v1, v1
	v_mov_b32_e32 v2, s3
	ds_read_b32 v226, v2
	s_mul_i32 s3, s63, s6
	s_sub_i32 s64, s2, s3
	s_lshl_b32 s99, s99, 1
	s_add_i32 s64, s64, s99
	s_waitcnt lgkmcnt(1)
	v_add_u32_e32 v202, s64, v1
	s_branch .LBB0_900

; #define LAS __attribute__((address_space(3)))
; #define FG_STAGE(bufoff, gbase, v0, v1) do { \
;         __builtin_amdgcn_global_load_lds((const unsigned*)((const char*)(gbase) + (v0)), (LAS unsigned*)(lds + (bufoff) + ldsw), 16, 0, 0); \
;         __builtin_amdgcn_global_load_lds((const unsigned*)((const char*)(gbase) + (v1)), (LAS unsigned*)(lds + (bufoff) + ldsw + 8192), 16, 0, 0); } while (0)
; #define FG_WAIT_V(n) asm volatile("s_waitcnt vmcnt(" #n ")" ::: "memory")
; #define FG_BAR __builtin_amdgcn_s_barrier()
;     __device__ __forceinline__ const char* a_base(const DUnit& u) const { return (const char*)(u.p ? A1 : A0) + (size_t)u.pm * 256 * K * 2; }
;     __device__ __forceinline__ const char* b_base(const DUnit& u) const { return (const char*)(u.p ? B1 : B0) + (size_t)u.pn * 256 * K * 2; }
;     __device__ __forceinline__ unsigned a_voff(const DUnit&, int row, int col) const { return (unsigned)(row * K + col) * 2u; }
;     __device__ __forceinline__ bool next(int i, SkUnit& u) const { const int L = i * G + c; if (L >= (T / 256) * 4) return false; u.pm = L >> 2; u.ks = L & 3; return true; }
; template <bool GATHER, class Unit, class Epi, class Sched>
; __device__ __forceinline__ void gemm_phase(LAS unsigned char* lds, const int K, const Sched& S, const Epi& E) {
;     ...
;     const char* cA = S.a_base(cur); const char* cB = S.b_base(cur);
;     unsigned vA00 = S.a_voff(cur, R0, C0), vA01 = S.a_voff(cur, R1, C1), vA10 = S.a_voff(cur, HALF + R0, C0), vA11 = S.a_voff(cur, HALF + R1, C1);
;     unsigned vN00 = vA00, vN01 = vA01, vN10 = vA10, vN11 = vA11;
;     bool hi_on = !S.lo_only(cur);
;     FG_STAGE(FG_SB(0, 0), cB, voffB0, voffB1); FG_STAGE(FG_SB(0, 1), cB + hstepB, voffB0, voffB1); FG_STAGE(FG_SA(0, 0), cA, vA00, vA01); FG_STAGE(FG_SA(0, 1), cA, vA10, vA11);
;     if (wr == 1) FG_BAR;
;     FG_WAIT_V(2); FG_BAR;
;     FG_STAGE(FG_SB(1, 0), cB + kstep, voffB0, voffB1); FG_STAGE(FG_SA(1, 0), cA + kstep, vA00, vA01); FG_STAGE(FG_SB(1, 1), cB + hstepB + kstep, voffB0, voffB1);
;     FG_WAIT_V(6); FG_BAR;
;     __device__ __forceinline__ bool next(int i, MUnit& u) const {
;         const LAS int* xs = (const LAS int*)((const LAS unsigned char*)ts + (LDS_XS - LDS_TS));
;         const int x = c & 7, W = G >> 3, q = i * W + (c >> 3); if ((G & 7) != 0 || q >= xs[8] * NPN) return false;
;         int k = 0; while (xs[k + 1] * NPN <= q) ++k;
.LBB0_902:
	s_add_u32 s18, s12, 0x4f100000
	s_addc_u32 s19, s13, 0
	s_add_u32 s50, s12, 0x4e200000
	s_mov_b64 s[20:21], 0x80
	s_addc_u32 s51, s13, 0
	s_lshl_b32 s6, s6, 12
	v_lshl_add_u64 v[6:7], v[6:7], 0, s[20:21]
	s_add_i32 m0, s27, 0x18000
	s_lshl_b32 s34, s7, 13
	s_and_b32 s35, s6, 0x3000
	s_waitcnt vmcnt(2)
	s_barrier
	global_load_lds_dwordx4 v[6:7], off
	s_add_i32 m0, s27, 0x1a000
	s_add_u32 s24, s12, 0x1be00080
	v_lshl_add_u64 v[4:5], v[4:5], 0, s[20:21]
	s_addc_u32 s25, s13, 0
	s_add_i32 s52, s27, 0x8000
	s_add_i32 s53, s27, 0xa000
	global_load_lds_dwordx4 v[4:5], off
	v_lshl_add_u64 v[4:5], s[24:25], 0, v[2:3]
	s_mov_b32 m0, s52
	s_add_u32 s6, s10, 0x80080
	global_load_lds_dwordx4 v[4:5], off
	v_lshl_add_u64 v[4:5], s[24:25], 0, v[208:209]
	s_mov_b32 m0, s53
	s_addc_u32 s7, s11, 0
	global_load_lds_dwordx4 v[4:5], off
	v_lshl_add_u64 v[4:5], s[6:7], 0, v[198:199]
	s_add_i32 m0, s27, 0x1c000
	v_and_b32_e32 v6, 48, v8
	global_load_lds_dwordx4 v[4:5], off
	v_lshl_add_u64 v[4:5], s[6:7], 0, v[200:201]
	s_add_i32 m0, s27, 0x1e000
	s_cmpk_lt_u32 s8, 0x100
	global_load_lds_dwordx4 v[4:5], off
	v_and_b32_e32 v5, 15, v8
	v_lshlrev_b32_e32 v8, 2, v8
	v_lshlrev_b32_e32 v5, 6, v5
	v_and_b32_e32 v8, 32, v8
	v_or_b32_e32 v7, v5, v6
	v_bitop3_b32 v5, v5, v8, v6 bitop3:0x36
	s_waitcnt vmcnt(6)
	v_bitop3_b32 v6, v7, s34, v8 bitop3:0xde
	v_or_b32_e32 v209, s35, v5
	v_cndmask_b32_e64 v5, 0, 1, s[4:5]
	v_subrev_u32_e32 v4, s9, v226
	s_cselect_b64 s[34:35], -1, 0
	s_ashr_i32 s54, s36, 3
	v_cmp_ne_u32_e64 s[4:5], 1, v5
	s_add_i32 s55, 0, 0x26f50
	s_add_i32 s56, 0, 0x26f14
	s_add_i32 s57, 0, 0x10000
	s_add_i32 s58, 0, 0x14000
	s_movk_i32 s59, 0xffc0
	s_movk_i32 s60, 0x81
	v_add_u32_e32 v223, 0, v6
	v_mov_b32_e32 v203, v2
	s_barrier
	s_branch .LBB0_905

; #define LAS __attribute__((address_space(3)))
;     __device__ __forceinline__ bool next(int i, SkUnit& u) const { const int L = i * G + c; if (L >= (T / 256) * 4) return false; u.pm = L >> 2; u.ks = L & 3; return true; }
;     __device__ __forceinline__ bool next(int i, MUnit& u) const {
;         const LAS int* xs = (const LAS int*)((const LAS unsigned char*)ts + (LDS_XS - LDS_TS));
;         const int x = c & 7, W = G >> 3, q = i * W + (c >> 3); if ((G & 7) != 0 || q >= xs[8] * NPN) return false;
;         int k = 0; while (xs[k + 1] * NPN <= q) ++k;
;         const int e = x + 8 * k, rq = q - xs[k] * NPN, nte = xs[k + 1] - xs[k]; u.pn = rq / nte; u.mt = rq - u.pn * nte;
;         u.e = e; u.mtg = ts[e] + u.mt; u.ce = cn[e]; return true; }
.LBB0_908:
	v_mov_b32_e32 v2, s8
	ds_read_b32 v2, v2
	s_add_i32 s7, s7, 1
	s_add_i32 s8, s8, 4
	s_waitcnt lgkmcnt(0)
	v_lshlrev_b32_e32 v5, 2, v2
	v_cmp_ge_i32_e32 vcc, s6, v5
	v_readfirstlane_b32 s9, v2
	s_cbranch_vccnz .LBB0_908
	s_lshl_b32 s8, s7, 2
	s_add_i32 s8, s8, 0
	s_add_i32 s8, s8, 0x26f10
	v_mov_b32_e32 v2, s8
	ds_read_b32 v2, v2
	s_lshr_b32 s99, s7, 3
	s_and_b32 s7, s7, 7
	s_lshl_b32 s7, s7, 3
	s_or_b32 s36, s7, s0
	s_waitcnt lgkmcnt(0)
	v_readfirstlane_b32 s8, v2
	s_sub_i32 s9, s9, s8
	s_abs_i32 s37, s9
	v_cvt_f32_u32_e32 v2, s37
	s_sub_i32 s38, 0, s37
	s_lshl_b32 s7, s8, 2
	s_sub_i32 s6, s6, s7
	v_rcp_iflag_f32_e32 v2, v2
	s_abs_i32 s8, s6
	s_xor_b32 s7, s6, s9
	s_ashr_i32 s7, s7, 31
	v_mul_f32_e32 v2, 0x4f7ffffe, v2
	v_cvt_u32_f32_e32 v2, v2
	s_nop 0
	v_readfirstlane_b32 s39, v2
	s_mul_i32 s38, s38, s39
	s_mul_hi_u32 s38, s39, s38
	s_add_i32 s39, s39, s38
	s_mul_hi_u32 s38, s8, s39
	s_mul_i32 s39, s38, s37
	s_sub_i32 s8, s8, s39
	s_add_i32 s41, s38, 1
	s_sub_i32 s39, s8, s37
	s_cmp_ge_u32 s8, s37
	s_cselect_b32 s38, s41, s38
	s_cselect_b32 s8, s39, s8
	s_add_i32 s39, s38, 1
	s_cmp_ge_u32 s8, s37
	s_cselect_b32 s8, s39, s38
	s_lshl_b32 s37, s36, 2
	s_xor_b32 s8, s8, s7
	s_add_i32 s37, s37, 0
	s_sub_i32 s61, s8, s7
	s_add_i32 s7, s37, 0x26c40
	v_mov_b32_e32 v2, s7
	s_add_i32 s7, s37, 0x26d50
	ds_read_b32 v2, v2
	v_mov_b32_e32 v5, s7
	ds_read_b32 v224, v5
	s_mul_i32 s7, s61, s9
	s_sub_i32 s62, s6, s7
	s_lshl_b32 s99, s99, 1
	s_add_i32 s62, s62, s99
	s_waitcnt lgkmcnt(0)
	v_add_u32_e32 v225, s62, v2
	s_mov_b64 s[8:9], -1

; __device__ __forceinline__ int obid() { int t = blockIdx.x; asm volatile("" : "+s"(t)); return t; }
; __device__ __forceinline__ void moe_prefix(LAS unsigned char* lds, const unsigned* cnt) {
;     ...
;     if (tz_ < 64) { const int e = tz_; const int c = (int)cnt[e], nt = (c + 255) >> 8;
;         int incl = nt;
; #pragma unroll
;         for (int o = 1; o < 64; o <<= 1) { const int up = __shfl_up(incl, o); if (e >= o) incl += up; }
;         const int excl = incl - nt;
;         s_ts[e] = excl; s_cn[e] = c;
;         for (int i = 0; i < nt; ++i) s_te[excl + i] = (unsigned char)e;
;         const int x = obid() & 7; int a2 = 0;
; #pragma unroll
;         for (int k = 0; k < 8; ++k) { const int tk = __shfl(nt, x + 8 * k); if (e == 0) s_xs[k] = a2; a2 += tk; }
;         if (e == 0) s_xs[8] = a2; }
.LBB0_1011:
	s_or_b64 exec, exec, s[8:9]
	s_mov_b32 s0, s79
	v_cmp_eq_u32_e32 vcc, 0, v6
	v_and_or_b32 v2, s0, 7, v7
	v_lshlrev_b32_e32 v2, 2, v2
	v_min_u32_e32 v3, 2, v1
	v_sub_u32_e32 v4, v1, v3
	ds_bpermute_b32 v8, v2, v3
	ds_bpermute_b32 v9, v2, v3 offset:32
	ds_bpermute_b32 v10, v2, v3 offset:64
	ds_bpermute_b32 v11, v2, v3 offset:96
	ds_bpermute_b32 v12, v2, v3 offset:128
	ds_bpermute_b32 v13, v2, v3 offset:160
	ds_bpermute_b32 v14, v2, v3 offset:192
	ds_bpermute_b32 v15, v2, v3 offset:224
	ds_bpermute_b32 v16, v2, v4
	ds_bpermute_b32 v17, v2, v4 offset:32
	ds_bpermute_b32 v18, v2, v4 offset:64
	ds_bpermute_b32 v19, v2, v4 offset:96
	ds_bpermute_b32 v20, v2, v4 offset:128
	ds_bpermute_b32 v21, v2, v4 offset:160
	ds_bpermute_b32 v22, v2, v4 offset:192
	ds_bpermute_b32 v23, v2, v4 offset:224
	s_waitcnt lgkmcnt(0)
	v_add_u32_e32 v9, v9, v8
	v_add_u32_e32 v10, v10, v9
	v_add_u32_e32 v11, v11, v10
	v_add_u32_e32 v12, v12, v11
	v_add_u32_e32 v13, v13, v12
	v_add_u32_e32 v14, v14, v13
	v_add_u32_e32 v15, v15, v14
	v_add_u32_e32 v16, v16, v15
	v_add_u32_e32 v17, v17, v16
	v_add_u32_e32 v18, v18, v17
	v_add_u32_e32 v19, v19, v18
	v_add_u32_e32 v20, v20, v19
	v_add_u32_e32 v21, v21, v20
	v_add_u32_e32 v22, v22, v21
	v_add_u32_e32 v23, v23, v22
	v_mov_b32_e32 v5, 0
	s_and_b64 exec, exec, vcc
	s_cbranch_execz .LBB0_1027
	v_mov_b32_e32 v3, 0x26f10
	ds_write2_b32 v3, v5, v8 offset1:1
	ds_write2_b32 v3, v9, v10 offset0:2 offset1:3
	ds_write2_b32 v3, v11, v12 offset0:4 offset1:5
	ds_write2_b32 v3, v13, v14 offset0:6 offset1:7
	ds_write2_b32 v3, v15, v16 offset0:8 offset1:9
	ds_write2_b32 v3, v17, v18 offset0:10 offset1:11
	ds_write2_b32 v3, v19, v20 offset0:12 offset1:13
	ds_write2_b32 v3, v21, v22 offset0:14 offset1:15
	ds_write_b32 v3, v23 offset:64

; #define LAS __attribute__((address_space(3)))
;     __device__ __forceinline__ bool next(int i, SkUnit& u) const { const int L = i * G + c; if (L >= (T / 256) * 4) return false; u.pm = L >> 2; u.ks = L & 3; return true; }
;     __device__ __forceinline__ bool next(int i, MUnit& u) const {
;         const LAS int* xs = (const LAS int*)((const LAS unsigned char*)ts + (LDS_XS - LDS_TS));
;         const int x = c & 7, W = G >> 3, q = i * W + (c >> 3); if ((G & 7) != 0 || q >= xs[8] * NPN) return false;
;         int k = 0; while (xs[k + 1] * NPN <= q) ++k;
;         const int e = x + 8 * k, rq = q - xs[k] * NPN, nte = xs[k + 1] - xs[k]; u.pn = rq / nte; u.mt = rq - u.pn * nte;
;         u.e = e; u.mtg = ts[e] + u.mt; u.ce = cn[e]; return true; }
.LBB0_1029:
	s_add_i32 s2, 0, 0x26f50
	v_mov_b32_e32 v2, s2
	ds_read_b32 v2, v2
	s_waitcnt lgkmcnt(0)
	v_lshlrev_b32_e32 v2, 3, v2
	v_cmp_ge_i32_e32 vcc, s1, v2
	s_cbranch_vccnz .LBB0_1033
	s_add_i32 s3, 0, 0x26f14
	s_mov_b32 s2, -1
.LBB0_1031:
	v_mov_b32_e32 v2, s3
	ds_read_b32 v2, v2
	s_add_i32 s2, s2, 1
	s_add_i32 s3, s3, 4
	s_waitcnt lgkmcnt(0)
	v_lshlrev_b32_e32 v3, 3, v2
	v_cmp_ge_i32_e32 vcc, s1, v3
	v_readfirstlane_b32 s6, v2
	s_cbranch_vccnz .LBB0_1031
	s_lshl_b32 s3, s2, 2
	s_add_i32 s3, s3, 0
	s_add_i32 s3, s3, 0x26f10
	v_mov_b32_e32 v2, s3
	ds_read_b32 v2, v2
	s_lshr_b32 s99, s2, 3
	s_and_b32 s2, s2, 7
	s_lshl_b32 s2, s2, 3
	s_or_b32 s10, s2, s0
	s_waitcnt lgkmcnt(0)
	v_readfirstlane_b32 s3, v2
	s_sub_i32 s6, s6, s3
	s_abs_i32 s7, s6
	v_cvt_f32_u32_e32 v2, s7
	s_sub_i32 s12, 0, s7
	s_lshl_b32 s2, s3, 3
	s_sub_i32 s2, s1, s2
	v_rcp_iflag_f32_e32 v2, v2
	s_abs_i32 s11, s2
	s_xor_b32 s3, s2, s6
	s_ashr_i32 s3, s3, 31
	v_mul_f32_e32 v2, 0x4f7ffffe, v2
	v_cvt_u32_f32_e32 v2, v2
	s_nop 0
	v_readfirstlane_b32 s13, v2
	s_mul_i32 s12, s12, s13
	s_mul_hi_u32 s12, s13, s12
	s_add_i32 s13, s13, s12
	s_mul_hi_u32 s12, s11, s13
	s_mul_i32 s13, s12, s7
	s_sub_i32 s11, s11, s13
	s_add_i32 s15, s12, 1
	s_sub_i32 s13, s11, s7
	s_cmp_ge_u32 s11, s7
	s_cselect_b32 s12, s15, s12
	s_cselect_b32 s11, s13, s11
	s_add_i32 s13, s12, 1
	s_cmp_ge_u32 s11, s7
	s_cselect_b32 s7, s13, s12
	s_lshl_b32 s11, s10, 2
	s_xor_b32 s7, s7, s3
	s_add_i32 s11, s11, 0
	s_sub_i32 s66, s7, s3
	s_add_i32 s3, s11, 0x26c40
	v_mov_b32_e32 v2, s3
	ds_read_b32 v2, v2
	s_add_i32 s3, s11, 0x26d50
	v_mov_b32_e32 v3, s3
	ds_read_b32 v224, v3
	s_mul_i32 s6, s66, s6
	s_sub_i32 s18, s2, s6
	s_lshl_b32 s99, s99, 1
	s_add_i32 s18, s18, s99
	s_waitcnt lgkmcnt(1)
	v_readfirstlane_b32 s2, v2
	s_add_i32 s46, s18, s2
	s_branch .LBB0_1034

; #define LAS __attribute__((address_space(3)))
; #define FG_STAGE(bufoff, gbase, v0, v1) do { \
;         __builtin_amdgcn_global_load_lds((const unsigned*)((const char*)(gbase) + (v0)), (LAS unsigned*)(lds + (bufoff) + ldsw), 16, 0, 0); \
;         __builtin_amdgcn_global_load_lds((const unsigned*)((const char*)(gbase) + (v1)), (LAS unsigned*)(lds + (bufoff) + ldsw + 8192), 16, 0, 0); } while (0)
; #define FG_WAIT_V(n) asm volatile("s_waitcnt vmcnt(" #n ")" ::: "memory")
; #define FG_BAR __builtin_amdgcn_s_barrier()
;     __device__ __forceinline__ const char* a_base(const DUnit& u) const { return (const char*)(u.p ? A1 : A0) + (size_t)u.pm * 256 * K * 2; }
;     __device__ __forceinline__ const char* b_base(const DUnit& u) const { return (const char*)(u.p ? B1 : B0) + (size_t)u.pn * 256 * K * 2; }
;     __device__ __forceinline__ unsigned a_voff(const DUnit&, int row, int col) const { return (unsigned)(row * K + col) * 2u; }
;     __device__ __forceinline__ bool next(int i, SkUnit& u) const { const int L = i * G + c; if (L >= (T / 256) * 4) return false; u.pm = L >> 2; u.ks = L & 3; return true; }
; template <bool GATHER, class Unit, class Epi, class Sched>
; __device__ __forceinline__ void gemm_phase(LAS unsigned char* lds, const int K, const Sched& S, const Epi& E) {
;     ...
;     const char* cA = S.a_base(cur); const char* cB = S.b_base(cur);
;     unsigned vA00 = S.a_voff(cur, R0, C0), vA01 = S.a_voff(cur, R1, C1), vA10 = S.a_voff(cur, HALF + R0, C0), vA11 = S.a_voff(cur, HALF + R1, C1);
;     unsigned vN00 = vA00, vN01 = vA01, vN10 = vA10, vN11 = vA11;
;     bool hi_on = !S.lo_only(cur);
;     FG_STAGE(FG_SB(0, 0), cB, voffB0, voffB1); FG_STAGE(FG_SB(0, 1), cB + hstepB, voffB0, voffB1); FG_STAGE(FG_SA(0, 0), cA, vA00, vA01); FG_STAGE(FG_SA(0, 1), cA, vA10, vA11);
;     if (wr == 1) FG_BAR;
;     FG_WAIT_V(2); FG_BAR;
;     FG_STAGE(FG_SB(1, 0), cB + kstep, voffB0, voffB1); FG_STAGE(FG_SA(1, 0), cA + kstep, vA00, vA01); FG_STAGE(FG_SB(1, 1), cB + hstepB + kstep, voffB0, voffB1);
;     FG_WAIT_V(6); FG_BAR;
;     __device__ __forceinline__ bool next(int i, MUnit& u) const {
;         const LAS int* xs = (const LAS int*)((const LAS unsigned char*)ts + (LDS_XS - LDS_TS));
;         const int x = c & 7, W = G >> 3, q = i * W + (c >> 3); if ((G & 7) != 0 || q >= xs[8] * NPN) return false;
;         int k = 0; while (xs[k + 1] * NPN <= q) ++k;
.LBB0_1036:
	s_lshl_b32 s19, s18, 8
	s_add_u32 s33, s4, 0x52100000
	s_addc_u32 s52, s5, 0
	s_add_u32 s53, s4, 0x4ec00000
	s_mov_b64 s[24:25], 0x80
	s_addc_u32 s54, s5, 0
	s_lshl_b32 s4, s15, 12
	v_lshl_add_u64 v[10:11], v[10:11], 0, s[24:25]
	s_add_i32 m0, s27, 0x18000
	s_lshl_b32 s17, s17, 13
	s_and_b32 s15, s4, 0x3000
	s_waitcnt vmcnt(2)
	s_barrier
	global_load_lds_dwordx4 v[10:11], off
	v_lshl_add_u64 v[8:9], v[8:9], 0, s[24:25]
	s_add_i32 m0, s27, 0x1a000
	s_add_i32 s55, s27, 0x8000
	s_add_i32 s56, s27, 0xa000
	global_load_lds_dwordx4 v[8:9], off
	v_lshl_add_u64 v[4:5], v[4:5], 0, s[24:25]
	s_mov_b32 m0, s55
	s_add_u32 s4, s12, 0x20080
	global_load_lds_dwordx4 v[4:5], off
	v_lshl_add_u64 v[4:5], v[6:7], 0, s[24:25]
	s_mov_b32 m0, s56
	s_addc_u32 s5, s13, 0
	global_load_lds_dwordx4 v[4:5], off
	v_lshl_add_u64 v[4:5], s[4:5], 0, v[198:199]
	s_add_i32 m0, s27, 0x1c000
	v_mov_b32_e32 v207, v3
	global_load_lds_dwordx4 v[4:5], off
	v_lshl_add_u64 v[4:5], s[4:5], 0, v[200:201]
	s_add_i32 m0, s27, 0x1e000
	s_cmpk_lt_u32 s14, 0x100
	global_load_lds_dwordx4 v[4:5], off
	v_and_b32_e32 v4, 15, v1
	v_and_b32_e32 v5, 48, v1
	v_lshlrev_b32_e32 v1, 2, v1
	v_lshlrev_b32_e32 v4, 6, v4
	v_and_b32_e32 v1, 32, v1
	v_or_b32_e32 v7, v4, v5
	v_bitop3_b32 v4, v4, v1, v5 bitop3:0x36
	v_bitop3_b32 v5, v7, s17, v1 bitop3:0xde
	v_or_b32_e32 v1, s15, v4
	v_lshlrev_b32_e32 v4, 13, v14
	v_and_b32_e32 v4, 0xffffc000, v4
	v_lshl_add_u32 v4, v15, 10, v4
	v_and_b32_e32 v7, 1, v14
	v_lshl_or_b32 v4, v7, 6, v4
	v_lshlrev_b32_e32 v7, 1, v16
	v_add3_u32 v210, v4, v7, s11
	v_lshlrev_b32_e32 v4, 13, v2
	v_and_b32_e32 v4, 0xffffc000, v4
	v_lshl_add_u32 v4, v12, 10, v4
	v_and_b32_e32 v2, 1, v2
	s_waitcnt vmcnt(6)
	v_lshl_or_b32 v2, v2, 6, v4
	v_lshlrev_b32_e32 v4, 1, v13
	s_cselect_b64 s[34:35], -1, 0
	v_add3_u32 v212, v2, v4, s11
	v_cndmask_b32_e64 v2, 0, 1, s[8:9]
	s_add_i32 s61, 0, 0x10000
	s_add_i32 s62, 0, 0x14000
	v_mov_b32_e32 v209, v3
	s_waitcnt lgkmcnt(0)
	v_subrev_u32_e32 v6, s19, v224
	s_ashr_i32 s57, s16, 3
	v_mov_b32_e32 v211, v3
	v_mov_b32_e32 v213, v3
	v_cmp_ne_u32_e64 s[4:5], 1, v2
	s_add_i32 s58, 0, 0x26f50
	s_add_i32 s59, 0, 0x26f14
	s_movk_i32 s60, 0x80
	v_add_u32_e32 v220, s61, v1
	v_add_u32_e32 v221, s62, v1
	v_add_u32_e32 v222, 0, v5
	s_movk_i32 s63, 0xffc0
	s_barrier
	s_branch .LBB0_1039

; #define LAS __attribute__((address_space(3)))
;     __device__ __forceinline__ bool next(int i, SkUnit& u) const { const int L = i * G + c; if (L >= (T / 256) * 4) return false; u.pm = L >> 2; u.ks = L & 3; return true; }
;     __device__ __forceinline__ bool next(int i, MUnit& u) const {
;         const LAS int* xs = (const LAS int*)((const LAS unsigned char*)ts + (LDS_XS - LDS_TS));
;         const int x = c & 7, W = G >> 3, q = i * W + (c >> 3); if ((G & 7) != 0 || q >= xs[8] * NPN) return false;
;         int k = 0; while (xs[k + 1] * NPN <= q) ++k;
;         const int e = x + 8 * k, rq = q - xs[k] * NPN, nte = xs[k + 1] - xs[k]; u.pn = rq / nte; u.mt = rq - u.pn * nte;
;         u.e = e; u.mtg = ts[e] + u.mt; u.ce = cn[e]; return true; }
.LBB0_1042:
	v_mov_b32_e32 v2, s11
	ds_read_b32 v2, v2
	s_add_i32 s9, s9, 1
	s_add_i32 s11, s11, 4
	s_waitcnt vmcnt(0) lgkmcnt(0)
	v_lshlrev_b32_e32 v4, 3, v2
	v_cmp_ge_i32_e32 vcc, s8, v4
	v_readfirstlane_b32 s14, v2
	s_cbranch_vccnz .LBB0_1042
	s_lshl_b32 s11, s9, 2
	s_add_i32 s11, s11, 0
	s_add_i32 s11, s11, 0x26f10
	v_mov_b32_e32 v2, s11
	ds_read_b32 v2, v2
	s_lshr_b32 s99, s9, 3
	s_and_b32 s9, s9, 7
	s_lshl_b32 s9, s9, 3
	s_or_b32 s36, s9, s0
	s_mov_b64 s[40:41], -1
	s_waitcnt lgkmcnt(0)
	v_readfirstlane_b32 s11, v2
	s_sub_i32 s14, s14, s11
	s_abs_i32 s15, s14
	v_cvt_f32_u32_e32 v2, s15
	s_sub_i32 s16, 0, s15
	s_lshl_b32 s9, s11, 3
	s_sub_i32 s8, s8, s9
	v_rcp_iflag_f32_e32 v2, v2
	s_abs_i32 s11, s8
	s_xor_b32 s9, s8, s14
	s_ashr_i32 s9, s9, 31
	v_mul_f32_e32 v2, 0x4f7ffffe, v2
	v_cvt_u32_f32_e32 v2, v2
	s_nop 0
	v_readfirstlane_b32 s17, v2
	s_mul_i32 s16, s16, s17
	s_mul_hi_u32 s16, s17, s16
	s_add_i32 s17, s17, s16
	s_mul_hi_u32 s16, s11, s17
	s_mul_i32 s17, s16, s15
	s_sub_i32 s11, s11, s17
	s_add_i32 s19, s16, 1
	s_sub_i32 s17, s11, s15
	s_cmp_ge_u32 s11, s15
	s_cselect_b32 s16, s19, s16
	s_cselect_b32 s11, s17, s11
	s_add_i32 s17, s16, 1
	s_cmp_ge_u32 s11, s15
	s_cselect_b32 s11, s17, s16
	s_lshl_b32 s15, s36, 2
	s_xor_b32 s11, s11, s9
	s_add_i32 s15, s15, 0
	s_sub_i32 s64, s11, s9
	s_add_i32 s9, s15, 0x26c40
	v_mov_b32_e32 v2, s9
	ds_read_b32 v2, v2
	s_add_i32 s9, s15, 0x26d50
	v_mov_b32_e32 v4, s9
	ds_read_b32 v223, v4
	s_mul_i32 s11, s64, s14
	s_sub_i32 s65, s8, s11
	s_lshl_b32 s99, s99, 1
	s_add_i32 s65, s65, s99
	s_waitcnt lgkmcnt(0)
	v_readfirstlane_b32 s8, v2
	s_add_i32 s38, s65, s8
